# hgrn chunk loop: per-row 64-bit VALU address chains replaced by one scalar base (vcc) + eight loop-invariant lane offsets
# baseline (speedup 1.0000x reference)
.LBB0_812:
	s_lshl_b32 s60, s74, 1
	s_and_b32 s76, s60, 0x700
	s_and_b32 s77, s60, 0xc0
	s_ashr_i32 s60, s75, 5
	s_ashr_i32 s61, s60, 31
	s_lshl_b64 s[60:61], s[60:61], 12
	s_add_u32 s62, s60, s67
	s_addc_u32 s63, s61, s68
	s_lshl_b64 s[62:63], s[62:63], 13
	v_readlane_b32 s80, v242, 16
	v_readlane_b32 s81, v242, 17
	s_add_u32 s62, s80, s62
	s_addc_u32 s63, s81, s63
	s_lshl_b32 s78, s75, 6
	v_readlane_b32 s84, v244, 23
	s_and_b32 s84, s78, 0x700
	v_lshl_add_u64 v[2:3], s[60:61], 0, v[50:51]
	s_add_u32 s62, s62, s84
	v_lshlrev_b64 v[2:3], 13, v[2:3]
	v_readlane_b32 s85, v244, 24
	s_addc_u32 s63, s63, 0
	v_lshl_add_u64 v[2:3], s[80:81], 0, v[2:3]
	v_lshl_add_u64 v[58:59], s[62:63], 0, v[194:195]
	s_mov_b64 s[100:101], s[62:63]
	v_mov_b32_e32 v247, v194
	v_add_u32_e32 v248, 0x2000, v194
	v_add_u32_e32 v249, 0x4000, v194
	v_add_u32_e32 v250, 0x6000, v194
	v_add_u32_e32 v251, 0x8000, v194
	v_add_u32_e32 v252, 0xa000, v194
	v_add_u32_e32 v253, 0xc000, v194
	v_add_u32_e32 v254, 0xe000, v194
	v_lshl_add_u64 v[2:3], v[2:3], 0, s[84:85]
	s_and_b32 s84, s78, 0xc0
	global_load_dword v105, v194, s[62:63]
	global_load_dword v107, v194, s[62:63] offset:2048
	s_movk_i32 s62, 0x2000
	v_lshl_add_u64 v[4:5], v[2:3], 0, s[84:85]
	v_add_co_u32_e32 v2, vcc, s62, v58
	s_movk_i32 s62, 0x4000
	s_nop 0
	v_addc_co_u32_e32 v3, vcc, 0, v59, vcc
	global_load_dword v106, v[2:3], off
	global_load_dword v108, v[2:3], off offset:2048
	v_add_co_u32_e32 v2, vcc, s62, v58
	s_movk_i32 s62, 0x6000
	s_nop 0
	v_addc_co_u32_e32 v3, vcc, 0, v59, vcc
	global_load_dword v109, v[2:3], off
	global_load_dword v110, v[2:3], off offset:2048
	v_add_co_u32_e32 v2, vcc, s62, v58
	s_mov_b32 s62, 0x8000
	s_nop 0
	v_addc_co_u32_e32 v3, vcc, 0, v59, vcc
	global_load_dword v111, v[2:3], off
	global_load_dword v112, v[2:3], off offset:2048
	v_add_co_u32_e32 v2, vcc, s62, v58
	s_mov_b32 s62, 0xa000
	s_nop 0
	v_addc_co_u32_e32 v3, vcc, 0, v59, vcc
	global_load_dword v113, v[2:3], off
	global_load_dword v115, v[2:3], off offset:2048
	v_add_co_u32_e32 v2, vcc, s62, v58
	s_mov_b32 s62, 0xc000
	s_nop 0
	v_addc_co_u32_e32 v3, vcc, 0, v59, vcc
	global_load_dword v114, v[2:3], off
	global_load_dword v116, v[2:3], off offset:2048
	v_add_co_u32_e32 v2, vcc, s62, v58
	s_mov_b32 s62, 0xe000
	s_nop 0
	v_addc_co_u32_e32 v3, vcc, 0, v59, vcc
	v_mov_b32_e32 v57, v195
	global_load_dword v117, v[2:3], off
	global_load_dword v118, v[2:3], off offset:2048
	v_add_co_u32_e32 v2, vcc, s62, v58
	v_lshl_add_u64 v[4:5], v[4:5], 0, v[56:57]
	s_mov_b64 s[62:63], 0x1000
	v_addc_co_u32_e32 v3, vcc, 0, v59, vcc
	v_lshl_add_u64 v[60:61], v[4:5], 0, s[62:63]
	s_movk_i32 s62, 0x1000
	v_add_co_u32_e32 v4, vcc, s62, v4
	global_load_dword v119, v[2:3], off
	s_nop 0
	global_load_dword v2, v[2:3], off offset:2048
	v_addc_co_u32_e32 v5, vcc, 0, v5, vcc
	global_load_dwordx2 v[18:19], v[4:5], off
	v_lshl_add_u64 v[4:5], v[54:55], 0, s[60:61]
	v_lshlrev_b64 v[4:5], 11, v[4:5]
	v_or_b32_e32 v3, s76, v4
	s_mov_b32 s79, s85
	v_or_b32_e32 v4, s77, v3
	v_mov_b32_e32 v64, 0
	v_writelane_b32 v244, s78, 23
	v_lshl_add_u64 v[62:63], v[52:53], 0, v[4:5]
	s_mov_b64 s[60:61], 0
	s_mov_b32 s76, 0x40000
	v_mov_b32_e32 v65, v64
	v_mov_b32_e32 v66, v64
	v_mov_b32_e32 v67, v64
	v_mov_b32_e32 v68, v64
	v_mov_b32_e32 v69, v64
	v_mov_b32_e32 v70, v64
	v_mov_b32_e32 v71, v64
	v_mov_b32_e32 v72, v64
	v_mov_b32_e32 v73, v64
	v_mov_b32_e32 v74, v64
	v_mov_b32_e32 v75, v64
	v_mov_b32_e32 v76, v64
	v_mov_b32_e32 v77, v64
	v_mov_b32_e32 v78, v64
	v_mov_b32_e32 v79, v64
	v_writelane_b32 v244, s79, 24
	s_waitcnt vmcnt(0)
	s_branch .LBB0_814

.LBB0_814:
	v_readlane_b32 s62, v244, 23
	s_cmp_lg_u32 s60, 0x7e0000
	v_readlane_b32 s63, v244, 24
	s_mov_b32 s79, s63
	s_cselect_b32 s78, s76, 0xfc0000
	v_writelane_b32 v244, s62, 23
	s_movk_i32 s77, 0x2000
	v_mov_b32_e32 v14, v112
	v_writelane_b32 v244, s63, 24
	s_lshl_b64 s[62:63], s[78:79], 1
	s_add_u32 vcc_lo, s100, s62
	s_addc_u32 vcc_hi, s101, s63
	v_mov_b32_e32 v15, v110
	v_mov_b32_e32 v16, v108
	v_mov_b32_e32 v17, v107
	v_mov_b32_e32 v23, v111
	v_mov_b32_e32 v24, v109
	v_mov_b32_e32 v25, v106
	v_mov_b32_e32 v26, v105
	global_load_dword v105, v247, vcc
	global_load_dword v107, v247, vcc offset:2048
	global_load_dword v106, v248, vcc
	global_load_dword v108, v248, vcc offset:2048
	global_load_dword v109, v249, vcc
	global_load_dword v110, v249, vcc offset:2048
	global_load_dword v111, v250, vcc
	global_load_dword v112, v250, vcc offset:2048
	v_mov_b32_e32 v3, v118
	v_mov_b32_e32 v12, v116
	v_mov_b32_e32 v13, v115
	v_mov_b32_e32 v20, v119
	v_mov_b32_e32 v126, v117
	v_mov_b32_e32 v21, v114
	v_mov_b32_e32 v22, v113
	global_load_dword v113, v251, vcc
	global_load_dword v115, v251, vcc offset:2048
	global_load_dword v114, v252, vcc
	global_load_dword v116, v252, vcc offset:2048
	global_load_dword v117, v253, vcc
	global_load_dword v118, v253, vcc offset:2048
	global_load_dword v119, v254, vcc
	global_load_dword v57, v254, vcc offset:2048
	v_lshl_add_u64 v[4:5], v[60:61], 0, s[62:63]
	global_load_dwordx2 v[80:81], v[4:5], off
	v_lshlrev_b32_e32 v137, 16, v21
	v_and_b32_e32 v138, 0xffff0000, v21
	v_lshlrev_b32_e32 v21, 16, v16
	v_and_b32_e32 v5, s0, v16
	v_and_b32_e32 v4, 0xffff0000, v17
	v_lshlrev_b32_e32 v129, 16, v25
	v_and_b32_e32 v130, 0xffff0000, v25
	v_lshlrev_b32_e32 v131, 16, v24
	v_and_b32_e32 v132, 0xffff0000, v24
	v_lshlrev_b32_e32 v133, 16, v23
	v_and_b32_e32 v134, 0xffff0000, v23
	v_lshlrev_b32_e32 v135, 16, v22
	v_and_b32_e32 v136, 0xffff0000, v22
	v_pk_mov_b32 v[22:23], v[20:21], v[4:5] op_sel:[1,0]
	v_lshlrev_b32_e32 v24, 16, v17
	v_and_b32_e32 v25, 0xffff0000, v16
	v_lshlrev_b32_e32 v127, 16, v26
	v_and_b32_e32 v128, 0xffff0000, v26
	v_pk_add_f32 v[26:27], v[22:23], 1.0 op_sel_hi:[1,0] neg_lo:[1,0] neg_hi:[1,0]
	v_pk_add_f32 v[28:29], v[24:25], 1.0 op_sel_hi:[1,0] neg_lo:[1,0] neg_hi:[1,0]
	v_lshlrev_b32_e32 v32, 16, v15
	v_and_b32_e32 v33, 0xffff0000, v15
	v_pk_mul_f32 v[30:31], v[26:27], v[28:29]
	v_pk_add_f32 v[4:5], v[32:33], 1.0 op_sel_hi:[1,0] neg_lo:[1,0] neg_hi:[1,0]
	v_lshlrev_b32_e32 v36, 16, v14
	v_and_b32_e32 v37, 0xffff0000, v14
	v_pk_mul_f32 v[34:35], v[4:5], v[30:31]
	v_pk_add_f32 v[4:5], v[36:37], 1.0 op_sel_hi:[1,0] neg_lo:[1,0] neg_hi:[1,0]
	v_lshlrev_b32_e32 v40, 16, v13
	v_and_b32_e32 v41, 0xffff0000, v13
	v_pk_mul_f32 v[38:39], v[4:5], v[34:35]
	v_pk_add_f32 v[4:5], v[40:41], 1.0 op_sel_hi:[1,0] neg_lo:[1,0] neg_hi:[1,0]
	v_lshlrev_b32_e32 v44, 16, v12
	v_and_b32_e32 v45, 0xffff0000, v12
	v_pk_mul_f32 v[42:43], v[4:5], v[38:39]
	v_pk_add_f32 v[4:5], v[44:45], 1.0 op_sel_hi:[1,0] neg_lo:[1,0] neg_hi:[1,0]
	v_lshlrev_b32_e32 v48, 16, v3
	v_and_b32_e32 v49, 0xffff0000, v3
	v_pk_mul_f32 v[46:47], v[4:5], v[42:43]
	v_pk_add_f32 v[4:5], v[48:49], 1.0 op_sel_hi:[1,0] neg_lo:[1,0] neg_hi:[1,0]
	v_lshlrev_b32_e32 v122, 16, v2
	v_and_b32_e32 v123, 0xffff0000, v2
	v_pk_mul_f32 v[120:121], v[4:5], v[46:47]
	v_pk_add_f32 v[2:3], v[122:123], 1.0 op_sel_hi:[1,0] neg_lo:[1,0] neg_hi:[1,0]
	v_lshlrev_b32_e32 v140, 16, v20
	v_pk_mul_f32 v[124:125], v[2:3], v[120:121]
	v_add_u32_e32 v2, s69, v1
	ds_write_b64 v2, v[124:125] offset:57856
	s_waitcnt lgkmcnt(0)
	s_barrier
	ds_read2st64_b64 v[2:5], v82 offset0:113 offset1:114
	ds_read2st64_b64 v[6:9], v82 offset0:115 offset1:116
	v_and_b32_e32 v141, 0xffff0000, v20
	s_mul_i32 s62, s47, 0x880
	v_lshlrev_b32_e32 v139, 16, v126
	s_waitcnt lgkmcnt(1)
	v_cndmask_b32_e64 v10, v3, 1.0, s[54:55]
	v_cndmask_b32_e64 v11, v2, 1.0, s[54:55]
	v_mul_f32_e32 v11, v11, v4
	v_mul_f32_e32 v10, v10, v5
	v_cndmask_b32_e64 v10, v10, 1.0, s[56:57]
	v_cndmask_b32_e64 v11, v11, 1.0, s[56:57]
	s_waitcnt lgkmcnt(0)
	v_mul_f32_e32 v11, v6, v11
	v_mul_f32_e32 v10, v7, v10
	v_cndmask_b32_e64 v14, v10, 1.0, s[58:59]
	v_cndmask_b32_e64 v10, v11, 1.0, s[58:59]
	v_mul_f32_e32 v15, v8, v10
	ds_read2st64_b64 v[10:13], v82 offset0:117 offset1:118
	v_mul_f32_e32 v14, v9, v14
	v_cndmask_b32_e64 v20, v14, 1.0, s[0:1]
	v_cndmask_b32_e64 v22, v15, 1.0, s[0:1]
	ds_read2st64_b64 v[14:17], v82 offset0:119 offset1:120
	s_waitcnt lgkmcnt(1)
	v_cndmask_b32_e64 v29, 1.0, v10, s[44:45]
	v_cndmask_b32_e64 v26, 1.0, v11, s[44:45]
	v_mul_f32_e32 v142, v29, v12
	v_mul_f32_e32 v143, v26, v13
	v_cndmask_b32_e64 v29, v29, v142, s[4:5]
	v_cndmask_b32_e64 v26, v26, v143, s[4:5]
	s_waitcnt lgkmcnt(0)
	v_mul_f32_e32 v142, v14, v29
	v_mul_f32_e32 v143, v15, v26
	v_cndmask_b32_e64 v29, v29, v142, s[6:7]
	v_rcp_f32_e32 v22, v22
	v_rcp_f32_e32 v20, v20
	v_cndmask_b32_e64 v26, v26, v143, s[6:7]
	v_mul_f32_e32 v142, v16, v29
	v_cndmask_b32_e64 v29, v29, v142, s[8:9]
	v_mul_f32_e32 v142, v17, v26
	v_cndmask_b32_e64 v26, v26, v142, s[8:9]
	v_cndmask_b32_e64 v29, v22, v29, s[0:1]
	v_cndmask_b32_e64 v142, v20, v26, s[0:1]
	v_mul_f32_e32 v22, v28, v29
	v_mul_f32_e32 v28, v27, v142
	v_mul_f32_e32 v30, v30, v29
	v_mul_f32_e32 v31, v31, v142
	v_rcp_f32_e32 v20, v22
	v_rcp_f32_e32 v143, v28
	v_rcp_f32_e32 v26, v30
	v_rcp_f32_e32 v27, v31
	v_mul_f32_e32 v144, v20, v24
	v_mul_f32_e32 v143, v143, v23
	v_mov_b32_e32 v24, v21
	v_mul_f32_e32 v22, v22, v127
	v_mul_f32_e32 v23, v28, v128
	v_pk_mul_f32 v[20:21], v[26:27], v[24:25]
	v_cvt_pk_bf16_f32 v22, v22, v23
	v_mul_f32_e32 v23, v30, v129
	v_mul_f32_e32 v24, v31, v130
	v_add_u32_e32 v28, s62, v83
	v_cvt_pk_bf16_f32 v23, v23, v24
	ds_write2_b32 v28, v22, v23 offset1:68
	v_cvt_pk_bf16_f32 v22, v144, v143
	v_cvt_pk_bf16_f32 v23, v20, v21
	v_add_u32_e32 v25, 0x4400, v28
	v_mul_f32_e32 v26, v34, v29
	v_mul_f32_e32 v27, v35, v142
	v_mul_f32_e32 v30, v38, v29
	v_mul_f32_e32 v31, v39, v142
	ds_write2_b32 v25, v22, v23 offset1:68
	v_rcp_f32_e32 v34, v26
	v_rcp_f32_e32 v35, v27
	v_rcp_f32_e32 v22, v30
	v_rcp_f32_e32 v23, v31
	v_mul_f32_e32 v26, v26, v131
	v_mul_f32_e32 v27, v27, v132
	v_cvt_pk_bf16_f32 v26, v26, v27
	v_mul_f32_e32 v27, v30, v133
	v_mul_f32_e32 v30, v31, v134
	v_cvt_pk_bf16_f32 v24, v143, v21
	v_mul_f32_e32 v21, v34, v32
	v_mul_f32_e32 v32, v35, v33
	v_pk_mul_f32 v[22:23], v[22:23], v[36:37]
	v_cvt_pk_bf16_f32 v27, v27, v30
	ds_write2_b32 v28, v26, v27 offset0:136 offset1:204
	v_cvt_pk_bf16_f32 v26, v21, v32
	v_cvt_pk_bf16_f32 v27, v22, v23
	v_mul_f32_e32 v30, v42, v29
	v_mul_f32_e32 v33, v46, v29
	v_mul_f32_e32 v34, v47, v142
	ds_write2_b32 v25, v26, v27 offset0:136 offset1:204
	v_cvt_pk_bf16_f32 v21, v21, v22
	v_rcp_f32_e32 v22, v30
	v_rcp_f32_e32 v26, v33
	v_rcp_f32_e32 v27, v34
	v_mul_f32_e32 v31, v43, v142
	v_rcp_f32_e32 v35, v31
	v_cvt_pk_bf16_f32 v25, v32, v23
	v_mul_f32_e32 v32, v22, v40
	v_pk_mul_f32 v[22:23], v[26:27], v[44:45]
	v_mul_f32_e32 v26, v30, v135
	v_mul_f32_e32 v27, v31, v136
	v_cvt_pk_bf16_f32 v26, v26, v27
	v_mul_f32_e32 v27, v33, v137
	v_mul_f32_e32 v30, v34, v138
	v_mul_f32_e32 v35, v35, v41
	v_cvt_pk_bf16_f32 v27, v27, v30
	v_add_u32_e32 v30, 0x400, v28
	ds_write2_b32 v30, v26, v27 offset0:16 offset1:84
	v_cvt_pk_bf16_f32 v26, v32, v35
	v_cvt_pk_bf16_f32 v27, v22, v23
	v_add_u32_e32 v31, 0x4800, v28
	ds_write2_b32 v31, v26, v27 offset0:16 offset1:84
	v_cvt_pk_bf16_f32 v22, v32, v22
	v_mul_f32_e32 v27, v120, v29
	v_mul_f32_e32 v32, v121, v142
	v_mul_f32_e32 v33, v124, v29
	v_mul_f32_e32 v34, v125, v142
	v_rcp_f32_e32 v36, v27
	v_rcp_f32_e32 v37, v32
	v_rcp_f32_e32 v28, v33
	v_rcp_f32_e32 v29, v34
	v_and_b32_e32 v126, 0xffff0000, v126
	v_mul_f32_e32 v27, v27, v139
	v_mul_f32_e32 v32, v32, v126
	v_cvt_pk_bf16_f32 v27, v27, v32
	v_mul_f32_e32 v32, v33, v140
	v_mul_f32_e32 v33, v34, v141
	v_cvt_pk_bf16_f32 v26, v35, v23
	v_mul_f32_e32 v23, v36, v48
	v_mul_f32_e32 v35, v37, v49
	v_pk_mul_f32 v[28:29], v[28:29], v[122:123]
	v_cvt_pk_bf16_f32 v32, v32, v33
	ds_write2_b32 v30, v27, v32 offset0:152 offset1:220
	v_cvt_pk_bf16_f32 v27, v23, v35
	v_cvt_pk_bf16_f32 v30, v28, v29
	v_cvt_pk_bf16_f32 v20, v144, v20
	ds_write2_b32 v31, v27, v30 offset0:152 offset1:220
	v_cvt_pk_bf16_f32 v23, v23, v28
	v_cvt_pk_bf16_f32 v27, v35, v29
	v_add_u32_e32 v28, s70, v84
	s_andn2_b64 vcc, exec, s[50:51]
	ds_write_b128 v28, v[20:23] offset:34816
	ds_write_b128 v28, v[24:27] offset:34960
	s_cbranch_vccnz .LBB0_816
	v_pk_mul_f32 v[10:11], v[10:11], v[12:13]
	v_pk_mul_f32 v[2:3], v[2:3], v[4:5]
	v_pk_mul_f32 v[10:11], v[10:11], v[14:15]
	v_pk_mul_f32 v[2:3], v[2:3], v[6:7]
	v_pk_mul_f32 v[10:11], v[10:11], v[16:17]
	v_pk_mul_f32 v[2:3], v[2:3], v[8:9]
	s_nop 0
	v_pk_mul_f32 v[4:5], v[2:3], v[10:11]
	ds_write2st64_b64 v85, v[2:3], v[10:11] offset0:121 offset1:122
	ds_write_b64 v85, v[4:5] offset:62976
